# r1 + phase A and C tile order: the XCD remap of the static tile order is no longer applied on top of the already XCD-major workgroup index, so each XCD works on an 8x3 / 8x4 block of tiles (11-12 oper
# baseline (speedup 1.0000x reference)
.LBB0_712:
	s_and_b64 vcc, exec, s[6:7]
	s_movk_i32 s86, 0x1800
	s_cbranch_vccz .LBB0_747
	s_add_u32 s22, s52, 0x3be00000
	s_addc_u32 s23, s53, 0
	s_mul_i32 s54, s90, 0xc00000
	s_mul_hi_i32 s2, s90, 0xc00000
	s_add_u32 s3, s52, s54
	s_addc_u32 s2, s53, s2
	s_add_u32 s24, s3, 0x200000
	s_addc_u32 s25, s2, 0
	s_waitcnt vmcnt(0)
	v_mov_b32_e32 v1, v0
	s_cmpk_lt_u32 s89, 0x180
	s_cselect_b64 s[2:3], -1, 0
	s_cmpk_gt_u32 s89, 0x17f
	v_readfirstlane_b32 s7, v1
	s_cbranch_scc1 .LBB0_715
	s_mov_b32 s6, s89
	s_mul_i32 s8, s6, 0xaaab
	s_lshr_b32 s8, s8, 22
	s_mul_i32 s9, s8, 0x60
	s_sub_i32 s6, s6, s9
	s_lshl_b32 s8, s8, 3
	s_bfe_u32 s10, s6, 0x50003
	s_and_b32 s6, s6, 7
	s_or_b32 s6, s6, s8
	s_and_b32 s46, s6, 0x1fff
	s_lshl_b64 s[8:9], s[46:47], 20
	s_add_u32 s16, s22, s8
	s_addc_u32 s17, s23, s9
	s_lshl_b32 s6, s10, 20
	s_add_u32 s18, s24, s6
	s_addc_u32 s19, s25, 0
	s_lshl_b32 s26, s46, 8
	s_lshl_b32 s6, s10, 8

.LBB0_721:
	s_add_i32 s39, s39, 1
	s_mul_i32 s2, s39, s38
	s_mul_hi_u32 s3, s39, s92
	s_add_i32 s3, s3, s2
	s_mul_i32 s2, s39, s92
	s_add_u32 s20, s2, s89
	s_addc_u32 s21, s3, 0
	v_cmp_gt_i64_e32 vcc, s[20:21], v[198:199]
	v_cmp_lt_i64_e64 s[2:3], s[20:21], v[196:197]
	s_cbranch_vccnz .LBB0_723
	s_mov_b32 s7, s20
	s_mul_hi_i32 s12, s7, 0x2aaaaaab
	s_lshr_b32 s13, s12, 31
	s_ashr_i32 s12, s12, 4
	s_add_i32 s12, s12, s13
	s_lshl_b32 s13, s12, 3
	s_sub_i32 s14, 32, s13
	s_min_i32 s14, s14, 8
	s_abs_i32 s15, s14
	v_cvt_f32_u32_e32 v2, s15
	s_sub_i32 s21, 0, s15
	s_mulk_i32 s12, 0x60
	s_sub_i32 s7, s7, s12
	v_rcp_iflag_f32_e32 v2, v2
	s_abs_i32 s12, s7
	s_xor_b32 s20, s7, s14
	s_ashr_i32 s20, s20, 31
	v_mul_f32_e32 v2, 0x4f7ffffe, v2
	v_cvt_u32_f32_e32 v2, v2
	s_nop 0
	v_readfirstlane_b32 s40, v2
	s_mul_i32 s21, s21, s40
	s_mul_hi_u32 s21, s40, s21
	s_add_i32 s40, s40, s21
	s_mul_hi_u32 s21, s12, s40
	s_mul_i32 s40, s21, s15
	s_sub_i32 s12, s12, s40
	s_add_i32 s41, s21, 1
	s_sub_i32 s40, s12, s15
	s_cmp_ge_u32 s12, s15
	s_cselect_b32 s21, s41, s21
	s_cselect_b32 s12, s40, s12
	s_add_i32 s40, s21, 1
	s_cmp_ge_u32 s12, s15
	s_cselect_b32 s12, s40, s21
	s_xor_b32 s12, s12, s20
	s_sub_i32 s20, s12, s20
	s_mul_i32 s12, s20, s14
	s_sub_i32 s7, s7, s12
	s_add_i32 s40, s13, s7
	s_ashr_i32 s41, s40, 31
	s_lshl_b64 s[12:13], s[40:41], 20
	s_add_u32 s12, s22, s12
	s_addc_u32 s13, s23, s13
	s_ashr_i32 s21, s20, 31
	s_lshl_b64 s[14:15], s[20:21], 20
	s_add_u32 s14, s24, s14
	s_addc_u32 s15, s25, s15
	s_lshl_b32 s41, s40, 8
	s_lshl_b32 s40, s20, 8

.LBB0_894:
	v_readlane_b32 s4, v242, 30
	s_mov_b32 s10, s4
	s_add_u32 s28, s2, 0x40e00000
	s_addc_u32 s29, s3, 0
	s_ashr_i32 s11, s10, 31
	s_lshl_b64 s[4:5], s[10:11], 23
	s_add_u32 s4, s2, s4
	s_addc_u32 s5, s3, s5
	s_add_u32 s30, s4, 0x3200000
	s_addc_u32 s31, s5, 0
	v_mov_b32_e32 v1, v0
	s_cmpk_lt_u32 s26, 0x100
	s_cselect_b64 s[6:7], -1, 0
	s_cmpk_gt_u32 s26, 0xff
	v_readfirstlane_b32 s14, v1
	s_cbranch_scc1 .LBB0_896
	s_lshr_b32 s4, s26, 6
	s_lshl_b32 s4, s4, 3
	s_and_b32 s5, s26, 7
	s_bfe_u32 s8, s26, 0x30003
	s_or_b32 s9, s4, s5
	s_lshl_b32 s4, s9, 20
	s_add_u32 s4, s28, s4
	s_addc_u32 s5, s29, 0
	s_lshl_b32 s11, s8, 20
	s_add_u32 s22, s30, s11
	s_addc_u32 s23, s31, 0
	s_lshl_b32 s49, s9, 8
	s_lshl_b32 s48, s8, 8
